# v40 + MoE gate/up GEMM: C=0 first-half copy for the first K-iteration, zero-fill removed
# speedup vs baseline: 1.0146x; 1.0028x over previous
; #define PG8_STAGEA(bufoff, gbase, h) do { if constexpr (GATHER) { PG8_STAGE(bufoff, gbase, vA[h]); } else { PG8_STAGE(bufoff, (gbase) + (h) * hstepA, voffA); } } while (0)
; #define PG8_WAIT_V(n) asm volatile("s_waitcnt vmcnt(" #n ")" ::: "memory")
; #define PG8_BAR __builtin_amdgcn_s_barrier()
; #define PG8_CALCA(u, vo) do { _Pragma("unroll") for (int _h = 0; _h < 2; ++_h) _Pragma("unroll") for (int _i = 0; _i < 2; ++_i) \
;         vo[_h][_i] = Sched::ABLK ? ((unsigned)S.arow(u, 0) * (unsigned)lda + voffA[_i] + (unsigned)_h * 8192u) : ((unsigned)S.arow(u, _h * HALF + Rr[_i]) * (unsigned)lda + C2[_i]); } while (0)
;     __device__ __forceinline__ int arow(const pg8::Unit& u, int r) const { if (GATHER && u.roff >= 0) { const int rr = r < u.nvalid ? r : u.nvalid - 1; return tokl[u.roff + rr]; } return -u.roff - 1 + r; }
; template <class Epi, class Sched>
; __device__ __forceinline__ void gemm_phase(const int tid, LAS unsigned char* lds, const char* Abase, const int lda, const int ldb, const int K, const Sched& S, const Epi& E) {
;     ...
;     if constexpr (GATHER) { PG8_CALCA(cur, vA); } else { cA = Abase + (size_t)S.arow(cur, 0) * lda + S.acolb(cur); }
;     const char* cB = cur.bptr;
;     PG8_STAGE(PG8_SB(0, 0), cB, voffB); PG8_STAGE(PG8_SB(0, 1), cB + hstepB, voffB); PG8_STAGEA(PG8_SA(0, 0), cA, 0); PG8_STAGEA(PG8_SA(0, 1), cA, 1);
;     if (wr == 1) PG8_BAR;
;     PG8_WAIT_V(2); PG8_BAR;
;     PG8_STAGE(PG8_SB(1, 0), cB + kstep, voffB); PG8_STAGEA(PG8_SA(1, 0), cA + kstepA, 0); PG8_STAGE(PG8_SB(1, 1), cB + hstepB + kstep, voffB);
;     PG8_WAIT_V(6); PG8_BAR;
;     ...
; #pragma unroll
;         for (int a = 0; a < 2; ++a)
; #pragma unroll
;             for (int b = 0; b < 2; ++b)
; #pragma unroll
;                 for (int m = 0; m < 4; ++m)
; #pragma unroll
;                     for (int n = 0; n < 2; ++n) acc[a][b][m][n] = (f32x4){0.f, 0.f, 0.f, 0.f};
;         cur = nxt; cB = nB; cA = nA; ++ui;
.LBB0_1564:
	s_add_u32 s87, s38, 0x3da00000
	s_addc_u32 s88, s39, 0
	s_and_b32 s9, s0, 3
	s_lshl_b32 s11, s1, 13
	s_lshl_b32 s22, s0, 5
	s_lshl_b32 s9, s9, 12
	s_add_u32 s38, s42, 0x80
	v_mov_b32_e32 v199, v3
	s_addc_u32 s39, s43, 0
	s_add_i32 m0, s73, 0x18000
	v_lshl_add_u64 v[6:7], s[38:39], 0, v[198:199]
	v_mov_b32_e32 v201, v3
	s_waitcnt vmcnt(2)
	s_barrier
	global_load_lds_dwordx4 v[6:7], off
	s_add_i32 m0, s73, 0x1a000
	v_lshl_add_u64 v[6:7], s[38:39], 0, v[200:201]
	s_add_u32 s38, s46, 0x80
	v_mov_b32_e32 v197, v3
	s_addc_u32 s39, s47, 0
	s_add_i32 s89, s73, 0x8000
	v_mov_b32_e32 v1, v3
	global_load_lds_dwordx4 v[6:7], off
	v_lshl_add_u64 v[6:7], s[38:39], 0, v[196:197]
	s_mov_b32 m0, s89
	s_add_i32 s90, s73, 0xa000
	global_load_lds_dwordx4 v[6:7], off
	v_lshl_add_u64 v[6:7], s[38:39], 0, v[0:1]
	s_add_u32 s38, s42, 0x20080
	s_mov_b32 m0, s90
	s_addc_u32 s39, s43, 0
	global_load_lds_dwordx4 v[6:7], off
	s_add_i32 m0, s73, 0x1c000
	v_lshl_add_u64 v[6:7], s[38:39], 0, v[198:199]
	global_load_lds_dwordx4 v[6:7], off
	v_lshl_add_u64 v[6:7], s[38:39], 0, v[200:201]
	s_add_i32 m0, s73, 0x1e000
	v_lshrrev_b32_e32 v1, 1, v251
	global_load_lds_dwordx4 v[6:7], off
	s_cmp_gt_i32 s25, 0
	v_and_b32_e32 v204, 24, v1
	v_lshlrev_b32_e32 v1, 6, v251
	s_cselect_b64 s[50:51], -1, 0
	s_add_i32 s91, s25, -2
	v_and_b32_e32 v5, 0x3c0, v1
	v_lshlrev_b32_e32 v6, 2, v251
	s_cmpk_lt_u32 s10, 0x100
	v_lshl_or_b32 v1, v204, 1, v5
	v_and_b32_e32 v6, 32, v6
	s_waitcnt vmcnt(6)
	s_cselect_b64 s[52:53], -1, 0
	s_bfe_u32 s92, s0, 0x10001
	v_readlane_b32 s0, v254, 45
	v_bitop3_b32 v7, s11, v1, v6 bitop3:0xf6
	v_lshl_or_b32 v206, s1, 12, v5
	v_lshl_add_u32 v197, v4, 2, s0
	v_readlane_b32 s0, v253, 53
	v_bitop3_b32 v1, s9, v1, v6 bitop3:0xf6
	s_mov_b32 s11, 0
	v_ashrrev_i32_e32 v207, 31, v206
	s_and_b32 s22, s22, 32
	v_mov_b32_e32 v205, v3
	v_add_u32_e32 v244, 0, v7
	s_mov_b32 s9, s0
	s_barrier
	v_readlane_b32 s1, v253, 54
	s_branch .LBB0_1567
.LBB0_1565:
	s_mov_b32 s9, s54
	s_mov_b32 s40, s94
	s_mov_b64 s[42:43], s[0:1]
	s_mov_b32 s11, s93

; #define PG8_STAGEA(bufoff, gbase, h) do { if constexpr (GATHER) { PG8_STAGE(bufoff, gbase, vA[h]); } else { PG8_STAGE(bufoff, (gbase) + (h) * hstepA, voffA); } } while (0)
; #define PG8_LDA(dst, b, h) do { _Pragma("unroll") for (int m = 0; m < 4; ++m) _Pragma("unroll") for (int k = 0; k < 2; ++k) dst[m][k] = *(const LAS bf16x8*)(lds + PG8_SA(b, h) + aoff + m * 2048 + k * 1024); } while (0)
; #define PG8_MM(ai, bj, At, Bt) do { if constexpr (Epi::F8MMA) PG8_MMA8(ai, bj, At, Bt##8); else PG8_MMA(ai, bj, At, Bt); } while (0)
; #define PG8_WAIT_V(n) asm volatile("s_waitcnt vmcnt(" #n ")" ::: "memory")
; #define PG8_WAIT_L(n) asm volatile("s_waitcnt lgkmcnt(" #n ")" ::: "memory")
; #define PG8_BAR __builtin_amdgcn_s_barrier()
; #define PG8_SCHED __builtin_amdgcn_sched_barrier(0)
; template <class Epi, class Sched>
; __device__ __forceinline__ void gemm_phase(const int tid, LAS unsigned char* lds, const char* Abase, const int lda, const int ldb, const int K, const Sched& S, const Epi& E) {
;     ...
;             PG8_LDB(B0, 0, 0); PG8_LDB(B1, 0, 1); PG8_SCHED; PG8_LDA(At, 0, 0); PG8_STAGEA(PG8_SA(1, 1), a1, 1);
;             if constexpr (GATHER) { if (last) {
; #pragma unroll
;                 for (int h = 0; h < 2; ++h)
; #pragma unroll
;                     for (int i = 0; i < 2; ++i) vA[h][i] = vAn[h][i]; } }
;             PG8_WAIT_V(8); PG8_WAIT_L(0); PG8_BAR; PG8_MM(0, 0, At, B0); PG8_MM(0, 1, At, B1); PG8_BAR; PG8_SCHED;
;             PG8_LDA(At, 0, 1); PG8_STAGE(PG8_SB(0, 0), b2, voffB); PG8_STAGE(PG8_SB(0, 1), b2 + hstepB, voffB); PG8_STAGEA(PG8_SA(0, 0), a2, 0);
;             PG8_WAIT_V(8); PG8_WAIT_L(0); PG8_BAR; PG8_MM(1, 0, At, B0); PG8_MM(1, 1, At, B1); PG8_BAR; PG8_SCHED;
.Lpeel_gu:
	s_add_i32 s41, s41, 2
	s_and_b64 s[64:65], s[66:67], exec
	s_cselect_b32 s65, 0, s62
	s_cselect_b32 s64, 0, s63
	s_add_u32 s70, s46, s65
	s_addc_u32 s71, s47, s64
	s_add_u32 s68, s42, s62
	s_addc_u32 s69, s43, s63
	s_add_u32 s64, s70, 0x80
	s_addc_u32 s65, s71, 0
	s_waitcnt vmcnt(8)
	s_and_b64 s[66:67], s[66:67], exec
	s_waitcnt lgkmcnt(0)
	s_cselect_b32 s66, s0, s68
	s_cselect_b32 s67, s1, s69
	s_add_u32 s68, s66, 0x80
	s_addc_u32 s69, s67, 0
	s_barrier
	s_setprio 1
	s_waitcnt lgkmcnt(0)
	v_mfma_scale_f32_16x16x128_f8f6f4 v[192:195], v[20:27], v[60:67], 0, v220, v216 op_sel_hi:[0,0,0]
	v_mfma_scale_f32_16x16x128_f8f6f4 v[188:191], v[28:35], v[60:67], 0, v220, v216 op_sel_hi:[0,0,0]
	v_mfma_scale_f32_16x16x128_f8f6f4 v[184:187], v[20:27], v[52:59], 0, v220, v216 op_sel_hi:[0,0,0]
	v_mfma_scale_f32_16x16x128_f8f6f4 v[180:183], v[28:35], v[52:59], 0, v220, v216 op_sel_hi:[0,0,0]
	v_mfma_scale_f32_16x16x128_f8f6f4 v[176:179], v[20:27], v[44:51], 0, v220, v216 op_sel_hi:[0,0,0]
	v_mfma_scale_f32_16x16x128_f8f6f4 v[172:175], v[28:35], v[44:51], 0, v220, v216 op_sel_hi:[0,0,0]
	v_mfma_scale_f32_16x16x128_f8f6f4 v[168:171], v[20:27], v[36:43], 0, v220, v216 op_sel_hi:[0,0,0]
	v_mfma_scale_f32_16x16x128_f8f6f4 v[164:167], v[28:35], v[36:43], 0, v220, v216 op_sel_hi:[0,0,0]
	s_setprio 0
	s_setprio 1
	v_mfma_scale_f32_16x16x128_f8f6f4 v[160:163], v[4:11], v[60:67], 0, v216, v216 op_sel_hi:[0,0,0]
	v_mfma_scale_f32_16x16x128_f8f6f4 v[156:159], v[12:19], v[60:67], 0, v216, v216 op_sel_hi:[0,0,0]
	v_mfma_scale_f32_16x16x128_f8f6f4 v[152:155], v[4:11], v[52:59], 0, v216, v216 op_sel_hi:[0,0,0]
	v_mfma_scale_f32_16x16x128_f8f6f4 v[148:151], v[12:19], v[52:59], 0, v216, v216 op_sel_hi:[0,0,0]
	v_mfma_scale_f32_16x16x128_f8f6f4 v[144:147], v[4:11], v[44:51], 0, v216, v216 op_sel_hi:[0,0,0]
	v_mfma_scale_f32_16x16x128_f8f6f4 v[140:143], v[12:19], v[44:51], 0, v216, v216 op_sel_hi:[0,0,0]
	v_mfma_scale_f32_16x16x128_f8f6f4 v[136:139], v[4:11], v[36:43], 0, v216, v216 op_sel_hi:[0,0,0]
	v_mfma_scale_f32_16x16x128_f8f6f4 v[132:135], v[12:19], v[36:43], 0, v216, v216 op_sel_hi:[0,0,0]
	s_setprio 0
	s_barrier
	s_mov_b32 m0, s76
	v_lshl_add_u64 v[228:229], s[66:67], 0, v[198:199]
	s_add_u32 vcc_lo, s66, 0x20000
	ds_read_b128 v[36:39], v244 offset:16384
	ds_read_b128 v[40:43], v244 offset:17408
	ds_read_b128 v[44:47], v244 offset:18432
	ds_read_b128 v[48:51], v244 offset:19456
	ds_read_b128 v[52:55], v244 offset:20480
	ds_read_b128 v[56:59], v244 offset:21504
	ds_read_b128 v[60:63], v244 offset:22528
	ds_read_b128 v[64:67], v244 offset:23552
	global_load_lds_dwordx4 v[228:229], off
	v_lshl_add_u64 v[228:229], s[66:67], 0, v[200:201]
	s_mov_b32 m0, s77
	s_addc_u32 vcc_hi, s67, 0
	global_load_lds_dwordx4 v[228:229], off
	v_lshl_add_u64 v[228:229], vcc, 0, v[198:199]
	s_mov_b32 m0, s78
	s_nop 0
	global_load_lds_dwordx4 v[228:229], off
	v_lshl_add_u64 v[228:229], vcc, 0, v[200:201]
	s_mov_b32 m0, s79
	s_nop 0
	global_load_lds_dwordx4 v[228:229], off
	s_mov_b32 m0, s73
	s_nop 0
	global_load_lds_dwordx4 v196, s[70:71]
	s_mov_b32 m0, s82
	s_nop 0
	global_load_lds_dwordx4 v0, s[70:71]
	s_waitcnt vmcnt(8)
	s_waitcnt lgkmcnt(0)
	s_barrier
	s_setprio 1
	s_waitcnt lgkmcnt(0)
	v_mfma_scale_f32_16x16x128_f8f6f4 v[128:131], v[20:27], v[36:43], 0, v220, v216 op_sel_hi:[0,0,0]
	v_mfma_scale_f32_16x16x128_f8f6f4 v[124:127], v[28:35], v[36:43], 0, v220, v216 op_sel_hi:[0,0,0]
	v_mfma_scale_f32_16x16x128_f8f6f4 v[120:123], v[20:27], v[44:51], 0, v220, v216 op_sel_hi:[0,0,0]
	v_mfma_scale_f32_16x16x128_f8f6f4 v[116:119], v[28:35], v[44:51], 0, v220, v216 op_sel_hi:[0,0,0]
	v_mfma_scale_f32_16x16x128_f8f6f4 v[112:115], v[20:27], v[52:59], 0, v220, v216 op_sel_hi:[0,0,0]
	v_mfma_scale_f32_16x16x128_f8f6f4 v[108:111], v[28:35], v[52:59], 0, v220, v216 op_sel_hi:[0,0,0]
	v_mfma_scale_f32_16x16x128_f8f6f4 v[104:107], v[20:27], v[60:67], 0, v220, v216 op_sel_hi:[0,0,0]
	v_mfma_scale_f32_16x16x128_f8f6f4 v[100:103], v[28:35], v[60:67], 0, v220, v216 op_sel_hi:[0,0,0]
	s_setprio 0
	s_setprio 1
	v_mfma_scale_f32_16x16x128_f8f6f4 v[96:99], v[4:11], v[36:43], 0, v216, v216 op_sel_hi:[0,0,0]
	v_mfma_scale_f32_16x16x128_f8f6f4 v[92:95], v[12:19], v[36:43], 0, v216, v216 op_sel_hi:[0,0,0]
	v_mfma_scale_f32_16x16x128_f8f6f4 v[88:91], v[4:11], v[44:51], 0, v216, v216 op_sel_hi:[0,0,0]
	v_mfma_scale_f32_16x16x128_f8f6f4 v[84:87], v[12:19], v[44:51], 0, v216, v216 op_sel_hi:[0,0,0]
	v_mfma_scale_f32_16x16x128_f8f6f4 v[80:83], v[4:11], v[52:59], 0, v216, v216 op_sel_hi:[0,0,0]
	v_mfma_scale_f32_16x16x128_f8f6f4 v[76:79], v[12:19], v[52:59], 0, v216, v216 op_sel_hi:[0,0,0]
	v_mfma_scale_f32_16x16x128_f8f6f4 v[72:75], v[4:11], v[60:67], 0, v216, v216 op_sel_hi:[0,0,0]
	v_mfma_scale_f32_16x16x128_f8f6f4 v[68:71], v[12:19], v[60:67], 0, v216, v216 op_sel_hi:[0,0,0]
	s_setprio 0
	s_barrier
	s_branch .Lmid_gu

; #define PG8_STAGEA(bufoff, gbase, h) do { if constexpr (GATHER) { PG8_STAGE(bufoff, gbase, vA[h]); } else { PG8_STAGE(bufoff, (gbase) + (h) * hstepA, voffA); } } while (0)
; #define PG8_LDA(dst, b, h) do { _Pragma("unroll") for (int m = 0; m < 4; ++m) _Pragma("unroll") for (int k = 0; k < 2; ++k) dst[m][k] = *(const LAS bf16x8*)(lds + PG8_SA(b, h) + aoff + m * 2048 + k * 1024); } while (0)
; #define PG8_MM(ai, bj, At, Bt) do { if constexpr (Epi::F8MMA) PG8_MMA8(ai, bj, At, Bt##8); else PG8_MMA(ai, bj, At, Bt); } while (0)
; #define PG8_WAIT_V(n) asm volatile("s_waitcnt vmcnt(" #n ")" ::: "memory")
; #define PG8_WAIT_L(n) asm volatile("s_waitcnt lgkmcnt(" #n ")" ::: "memory")
; #define PG8_BAR __builtin_amdgcn_s_barrier()
; #define PG8_SCHED __builtin_amdgcn_sched_barrier(0)
; template <class Epi, class Sched>
; __device__ __forceinline__ void gemm_phase(const int tid, LAS unsigned char* lds, const char* Abase, const int lda, const int ldb, const int K, const Sched& S, const Epi& E) {
;     ...
;             PG8_LDB(B0, 1, 0); PG8_LDB(B1, 1, 1); PG8_SCHED; PG8_LDA(At, 1, 0); PG8_STAGEA(PG8_SA(0, 1), a2, 1);
;             PG8_WAIT_V(8); PG8_WAIT_L(0); PG8_BAR; PG8_MM(0, 0, At, B0); PG8_MM(0, 1, At, B1); PG8_BAR; PG8_SCHED;
;             PG8_LDA(At, 1, 1); PG8_STAGE(PG8_SB(1, 0), b3, voffB); PG8_STAGE(PG8_SB(1, 1), b3 + hstepB, voffB); PG8_STAGEA(PG8_SA(1, 0), a3, 0);
;             PG8_WAIT_V(8); PG8_WAIT_L(0); PG8_BAR; PG8_MM(1, 0, At, B0); PG8_MM(1, 1, At, B1); PG8_BAR; PG8_SCHED;
;         }
.Lmid_gu:
	s_add_i32 vcc_lo, 0, 0x18000
	s_add_i32 vcc_hi, 0, 0x1c000
	v_add_u32_e32 v16, vcc_lo, v1
	v_add_u32_e32 v32, vcc_hi, v1
	ds_read_b128 v[4:7], v16
	ds_read_b128 v[8:11], v16 offset:1024
	ds_read_b128 v[12:15], v16 offset:2048
	ds_read_b128 v[16:19], v16 offset:3072
	ds_read_b128 v[20:23], v32
	ds_read_b128 v[24:27], v32 offset:1024
	ds_read_b128 v[28:31], v32 offset:2048
	ds_read_b128 v[32:35], v32 offset:3072
	s_mov_b32 m0, s83
	v_lshl_add_u64 v[214:215], s[70:71], 0, v[214:215]
	ds_read_b128 v[36:39], v244 offset:32768
	ds_read_b128 v[40:43], v244 offset:33792
	ds_read_b128 v[44:47], v244 offset:34816
	ds_read_b128 v[48:51], v244 offset:35840
	ds_read_b128 v[52:55], v244 offset:36864
	ds_read_b128 v[56:59], v244 offset:37888
	ds_read_b128 v[60:63], v244 offset:38912
	ds_read_b128 v[64:67], v244 offset:39936
	global_load_lds_dwordx4 v[214:215], off
	v_lshl_add_u64 v[212:213], s[70:71], 0, v[212:213]
	s_mov_b32 m0, s86
	s_nop 0
	global_load_lds_dwordx4 v[212:213], off
	s_waitcnt vmcnt(8)
	s_waitcnt lgkmcnt(0)
	s_barrier
	s_setprio 1
	s_waitcnt lgkmcnt(0)
	v_mfma_scale_f32_16x16x128_f8f6f4 v[192:195], v[4:11], v[36:43], v[192:195], v220, v216 op_sel_hi:[0,0,0]
	v_mfma_scale_f32_16x16x128_f8f6f4 v[188:191], v[12:19], v[36:43], v[188:191], v220, v216 op_sel_hi:[0,0,0]
	v_mfma_scale_f32_16x16x128_f8f6f4 v[184:187], v[4:11], v[44:51], v[184:187], v220, v216 op_sel_hi:[0,0,0]
	v_mfma_scale_f32_16x16x128_f8f6f4 v[180:183], v[12:19], v[44:51], v[180:183], v220, v216 op_sel_hi:[0,0,0]
	v_mfma_scale_f32_16x16x128_f8f6f4 v[176:179], v[4:11], v[52:59], v[176:179], v220, v216 op_sel_hi:[0,0,0]
	v_mfma_scale_f32_16x16x128_f8f6f4 v[172:175], v[12:19], v[52:59], v[172:175], v220, v216 op_sel_hi:[0,0,0]
	v_mfma_scale_f32_16x16x128_f8f6f4 v[168:171], v[4:11], v[60:67], v[168:171], v220, v216 op_sel_hi:[0,0,0]
	v_mfma_scale_f32_16x16x128_f8f6f4 v[164:167], v[12:19], v[60:67], v[164:167], v220, v216 op_sel_hi:[0,0,0]
	s_setprio 0
	s_setprio 1
	v_mfma_scale_f32_16x16x128_f8f6f4 v[160:163], v[20:27], v[36:43], v[160:163], v216, v216 op_sel_hi:[0,0,0]
	v_mfma_scale_f32_16x16x128_f8f6f4 v[156:159], v[28:35], v[36:43], v[156:159], v216, v216 op_sel_hi:[0,0,0]
	v_mfma_scale_f32_16x16x128_f8f6f4 v[152:155], v[20:27], v[44:51], v[152:155], v216, v216 op_sel_hi:[0,0,0]
	v_mfma_scale_f32_16x16x128_f8f6f4 v[148:151], v[28:35], v[44:51], v[148:151], v216, v216 op_sel_hi:[0,0,0]
	v_mfma_scale_f32_16x16x128_f8f6f4 v[144:147], v[20:27], v[52:59], v[144:147], v216, v216 op_sel_hi:[0,0,0]
	v_mfma_scale_f32_16x16x128_f8f6f4 v[140:143], v[28:35], v[52:59], v[140:143], v216, v216 op_sel_hi:[0,0,0]
	v_mfma_scale_f32_16x16x128_f8f6f4 v[136:139], v[20:27], v[60:67], v[136:139], v216, v216 op_sel_hi:[0,0,0]
	v_mfma_scale_f32_16x16x128_f8f6f4 v[132:135], v[28:35], v[60:67], v[132:135], v216, v216 op_sel_hi:[0,0,0]
	s_setprio 0
	s_barrier
	s_add_i32 s70, vcc_lo, s72
	v_lshl_add_u64 v[212:213], s[68:69], 0, v[198:199]
	s_mov_b32 m0, s70
	ds_read_b128 v[36:39], v244 offset:49152
	ds_read_b128 v[40:43], v244 offset:50176
	ds_read_b128 v[44:47], v244 offset:51200
	ds_read_b128 v[48:51], v244 offset:52224
	ds_read_b128 v[52:55], v244 offset:53248
	ds_read_b128 v[56:59], v244 offset:54272
	ds_read_b128 v[60:63], v244 offset:55296
	ds_read_b128 v[64:67], v244 offset:56320
	global_load_lds_dwordx4 v[212:213], off
	s_add_i32 m0, s70, 0x2000
	s_add_u32 s66, s66, 0x20080
	v_lshl_add_u64 v[212:213], s[68:69], 0, v[200:201]
	s_addc_u32 s67, s67, 0
	s_add_i32 s68, vcc_hi, s72
	global_load_lds_dwordx4 v[212:213], off
	v_lshl_add_u64 v[212:213], s[66:67], 0, v[198:199]
	s_mov_b32 m0, s68
	s_nop 0
	global_load_lds_dwordx4 v[212:213], off
	v_lshl_add_u64 v[212:213], s[66:67], 0, v[200:201]
	s_add_i32 m0, s68, 0x2000
	s_nop 0
	global_load_lds_dwordx4 v[212:213], off
	s_mov_b32 m0, s89
	s_nop 0
	global_load_lds_dwordx4 v196, s[64:65]
	s_mov_b32 m0, s90
	s_nop 0
	global_load_lds_dwordx4 v0, s[64:65]
	s_waitcnt vmcnt(8)
	s_waitcnt lgkmcnt(0)
	s_barrier
	s_setprio 1
	s_waitcnt lgkmcnt(0)
	v_mfma_scale_f32_16x16x128_f8f6f4 v[128:131], v[4:11], v[36:43], v[128:131], v220, v216 op_sel_hi:[0,0,0]
	v_mfma_scale_f32_16x16x128_f8f6f4 v[124:127], v[12:19], v[36:43], v[124:127], v220, v216 op_sel_hi:[0,0,0]
	v_mfma_scale_f32_16x16x128_f8f6f4 v[120:123], v[4:11], v[44:51], v[120:123], v220, v216 op_sel_hi:[0,0,0]
	v_mfma_scale_f32_16x16x128_f8f6f4 v[116:119], v[12:19], v[44:51], v[116:119], v220, v216 op_sel_hi:[0,0,0]
	v_mfma_scale_f32_16x16x128_f8f6f4 v[112:115], v[4:11], v[52:59], v[112:115], v220, v216 op_sel_hi:[0,0,0]
	v_mfma_scale_f32_16x16x128_f8f6f4 v[108:111], v[12:19], v[52:59], v[108:111], v220, v216 op_sel_hi:[0,0,0]
	v_mfma_scale_f32_16x16x128_f8f6f4 v[104:107], v[4:11], v[60:67], v[104:107], v220, v216 op_sel_hi:[0,0,0]
	v_mfma_scale_f32_16x16x128_f8f6f4 v[100:103], v[12:19], v[60:67], v[100:103], v220, v216 op_sel_hi:[0,0,0]
	s_setprio 0
	s_setprio 1
	v_mfma_scale_f32_16x16x128_f8f6f4 v[96:99], v[20:27], v[36:43], v[96:99], v216, v216 op_sel_hi:[0,0,0]
	v_mfma_scale_f32_16x16x128_f8f6f4 v[92:95], v[28:35], v[36:43], v[92:95], v216, v216 op_sel_hi:[0,0,0]
	v_mfma_scale_f32_16x16x128_f8f6f4 v[88:91], v[20:27], v[44:51], v[88:91], v216, v216 op_sel_hi:[0,0,0]
	v_mfma_scale_f32_16x16x128_f8f6f4 v[84:87], v[28:35], v[44:51], v[84:87], v216, v216 op_sel_hi:[0,0,0]
	v_mfma_scale_f32_16x16x128_f8f6f4 v[80:83], v[20:27], v[52:59], v[80:83], v216, v216 op_sel_hi:[0,0,0]
	v_mfma_scale_f32_16x16x128_f8f6f4 v[76:79], v[28:35], v[52:59], v[76:79], v216, v216 op_sel_hi:[0,0,0]
	v_mfma_scale_f32_16x16x128_f8f6f4 v[72:75], v[20:27], v[60:67], v[72:75], v216, v216 op_sel_hi:[0,0,0]
	v_mfma_scale_f32_16x16x128_f8f6f4 v[68:71], v[28:35], v[60:67], v[68:71], v216, v216 op_sel_hi:[0,0,0]
	s_setprio 0
	s_barrier
	s_add_u32 s62, s62, 0x100
	s_addc_u32 s63, s63, 0
	s_cmp_ge_i32 s41, s25
	s_cbranch_scc1 .LBB0_1598
; #define PG8_STAGEA(bufoff, gbase, h) do { if constexpr (GATHER) { PG8_STAGE(bufoff, gbase, vA[h]); } else { PG8_STAGE(bufoff, (gbase) + (h) * hstepA, voffA); } } while (0)
; #define PG8_LDA(dst, b, h) do { _Pragma("unroll") for (int m = 0; m < 4; ++m) _Pragma("unroll") for (int k = 0; k < 2; ++k) dst[m][k] = *(const LAS bf16x8*)(lds + PG8_SA(b, h) + aoff + m * 2048 + k * 1024); } while (0)
; #define PG8_SCHED __builtin_amdgcn_sched_barrier(0)
; template <class Epi, class Sched>
; __device__ __forceinline__ void gemm_phase(const int tid, LAS unsigned char* lds, const char* Abase, const int lda, const int ldb, const int K, const Sched& S, const Epi& E) {
;     ...
;         for (int t = 0; t < nt; t += 2) {
;             const bool last = (t == nt - 2);
;             const char* a1 = cA + (size_t)(t + 1) * kstepA;
;             const char* a2 = last ? nA : cA + (size_t)(t + 2) * kstepA; const char* b2 = last ? nB : cB + (size_t)(t + 2) * kstep;
;             const char* a3 = a2 + kstepA; const char* b3 = b2 + kstep;
;             PG8_LDB(B0, 0, 0); PG8_LDB(B1, 0, 1); PG8_SCHED; PG8_LDA(At, 0, 0); PG8_STAGEA(PG8_SA(1, 1), a1, 1);
.LBB0_1596:
	v_add_u32_e32 v4, 0, v1
	v_add_u32_e32 v5, 0x10000, v4
	v_add_u32_e32 v16, 0x14000, v4
	ds_read_b128 v[20:23], v5
	ds_read_b128 v[24:27], v5 offset:1024
	ds_read_b128 v[28:31], v5 offset:2048
	ds_read_b128 v[32:35], v5 offset:3072
	ds_read_b128 v[4:7], v16
	ds_read_b128 v[8:11], v16 offset:1024
	ds_read_b128 v[12:15], v16 offset:2048
	ds_read_b128 v[16:19], v16 offset:3072
	s_cmp_eq_u32 s91, s41
	s_cselect_b64 s[66:67], -1, 0
	s_add_u32 s64, s46, s62
	s_addc_u32 s65, s47, s63
	s_add_u32 s64, s64, 0xffffff80
	s_addc_u32 s65, s65, -1
	s_add_i32 m0, s73, 0xc000
	s_add_i32 s68, s73, 0xe000
	s_cmp_lg_u32 s91, s41
	ds_read_b128 v[60:63], v244
	ds_read_b128 v[64:67], v244 offset:1024
	ds_read_b128 v[52:55], v244 offset:2048
	ds_read_b128 v[56:59], v244 offset:3072
	ds_read_b128 v[44:47], v244 offset:4096
	ds_read_b128 v[48:51], v244 offset:5120
	ds_read_b128 v[36:39], v244 offset:6144
	ds_read_b128 v[40:43], v244 offset:7168
	global_load_lds_dwordx4 v2, s[64:65]
	s_mov_b32 m0, s68
	s_nop 0
	global_load_lds_dwordx4 v202, s[64:65]
	s_cbranch_scc0 .LBB0_1594
	v_mov_b32_e32 v203, v3
	v_mov_b64_e32 v[212:213], v[202:203]
	v_mov_b64_e32 v[214:215], v[2:3]
	s_cmp_eq_u32 s41, 0
	s_cbranch_scc1 .Lpeel_gu
	s_branch .LBB0_1595
